# v83 + P11 merge of the partner half-wave's top-16: elementwise max with the reversed list + bitonic merge (97 instructions instead of 534)
# baseline (speedup 1.0000x reference)
; __device__ __forceinline__ void p11_route(Frame& F) {
;     ...
;     for (int item = F.gw; item < (S_ / 16) * PH; item += F.NGW) {
;         const int tile = item >> 3, h = item & 7, t0 = tile * 16;
; #pragma unroll
;         for (int c = 0; c < 2; ++c) {
;             f32x4 acc[8];
; #pragma unroll
;             for (int nt = 0; nt < 8; ++nt) acc[nt] = (f32x4){0.f, 0.f, 0.f, 0.f};
; #pragma unroll
;             for (int ks = 0; ks < 4; ++ks) { const gbf16x8 a = *(const gbf16x8*)(QRY + (size_t)(t0 + l15) * 2048 + h * 256 + c * 128 + 32 * ks + 8 * g);
; #pragma unroll
;                 for (int nt = 0; nt < 8; ++nt) acc[nt] = __builtin_amdgcn_mfma_f32_16x16x32_bf16(a, *(const gbf16x8*)(SK + ((size_t)(h * 2 + c) * PNK + 16 * nt + l15) * 128 + 32 * ks + 8 * g), acc[nt], 0, 0, 0); }
.LBB0_3214:
	s_lshl_b32 s4, s17, 1
	s_and_b32 s18, s4, -16
	s_waitcnt lgkmcnt(0)
	v_or_b32_e32 v126, s18, v150
	v_ashrrev_i32_e32 v127, 31, v126
	v_lshlrev_b64 v[126:127], 12, v[126:127]
	v_lshl_add_u64 v[126:127], v[2:3], 0, v[126:127]
	global_load_dwordx4 v[128:131], v[126:127], off
	global_load_dwordx4 v[132:135], v[4:5], off
	global_load_dwordx4 v[136:139], v[6:7], off
	global_load_dwordx4 v[140:143], v[8:9], off
	global_load_dwordx4 v[144:147], v[10:11], off
	global_load_dwordx4 v[160:163], v[12:13], off
	global_load_dwordx4 v[164:167], v[14:15], off
	global_load_dwordx4 v[168:171], v[16:17], off
	global_load_dwordx4 v[172:175], v[18:19], off
	global_load_dwordx4 v[176:179], v[126:127], off offset:64
	global_load_dwordx4 v[180:183], v[4:5], off offset:64
	global_load_dwordx4 v[184:187], v[20:21], off
	global_load_dwordx4 v[188:191], v[22:23], off
	global_load_dwordx4 v[192:195], v[24:25], off
	global_load_dwordx4 v[196:199], v[26:27], off
	global_load_dwordx4 v[200:203], v[28:29], off
	global_load_dwordx4 v[204:207], v[30:31], off
	global_load_dwordx4 v[208:211], v[32:33], off
	global_load_dwordx4 v[212:215], v[126:127], off offset:128
	global_load_dwordx4 v[216:219], v[4:5], off offset:128
	global_load_dwordx4 v[220:223], v[34:35], off
	global_load_dwordx4 v[224:227], v[36:37], off
	global_load_dwordx4 v[228:231], v[38:39], off
	global_load_dwordx4 v[232:235], v[40:41], off
	global_load_dwordx4 v[236:239], v[42:43], off
	global_load_dwordx4 v[240:243], v[44:45], off
	global_load_dwordx4 v[244:247], v[46:47], off
	s_mov_b32 s4, 0
	v_mov_b32_e32 v148, 0xff800000
	v_mov_b32_e32 v149, 0xff800000
	v_mov_b32_e32 v159, 0xff800000
	s_waitcnt vmcnt(25)
	v_mfma_f32_16x16x32_bf16 v[132:135], v[128:131], v[132:135], 0
	s_waitcnt vmcnt(24)
	v_mfma_f32_16x16x32_bf16 v[136:139], v[128:131], v[136:139], 0
	s_waitcnt vmcnt(23)
	v_mfma_f32_16x16x32_bf16 v[140:143], v[128:131], v[140:143], 0
	s_waitcnt vmcnt(22)
	v_mfma_f32_16x16x32_bf16 v[144:147], v[128:131], v[144:147], 0
	s_waitcnt vmcnt(21)
	v_mfma_f32_16x16x32_bf16 v[160:163], v[128:131], v[160:163], 0
	s_waitcnt vmcnt(20)
	v_mfma_f32_16x16x32_bf16 v[164:167], v[128:131], v[164:167], 0
	s_waitcnt vmcnt(19)
	v_mfma_f32_16x16x32_bf16 v[168:171], v[128:131], v[168:171], 0
	s_waitcnt vmcnt(18)
	v_mfma_f32_16x16x32_bf16 v[128:131], v[128:131], v[172:175], 0
	s_waitcnt vmcnt(16)
	v_mfma_f32_16x16x32_bf16 v[132:135], v[176:179], v[180:183], v[132:135]
	s_waitcnt vmcnt(15)
	v_mfma_f32_16x16x32_bf16 v[136:139], v[176:179], v[184:187], v[136:139]
	s_waitcnt vmcnt(14)
	v_mfma_f32_16x16x32_bf16 v[140:143], v[176:179], v[188:191], v[140:143]
	s_waitcnt vmcnt(13)
	v_mfma_f32_16x16x32_bf16 v[144:147], v[176:179], v[192:195], v[144:147]
	s_waitcnt vmcnt(12)
	v_mfma_f32_16x16x32_bf16 v[160:163], v[176:179], v[196:199], v[160:163]
	s_waitcnt vmcnt(11)
	v_mfma_f32_16x16x32_bf16 v[164:167], v[176:179], v[200:203], v[164:167]
	s_waitcnt vmcnt(10)
	v_mfma_f32_16x16x32_bf16 v[168:171], v[176:179], v[204:207], v[168:171]
	s_waitcnt vmcnt(9)
	v_mfma_f32_16x16x32_bf16 v[128:131], v[176:179], v[208:211], v[128:131]
	global_load_dwordx4 v[176:179], v[126:127], off offset:192
	global_load_dwordx4 v[180:183], v[4:5], off offset:192
	global_load_dwordx4 v[184:187], v[48:49], off
	global_load_dwordx4 v[188:191], v[50:51], off
	global_load_dwordx4 v[192:195], v[52:53], off
	global_load_dwordx4 v[196:199], v[54:55], off
	global_load_dwordx4 v[200:203], v[56:57], off
	global_load_dwordx4 v[204:207], v[58:59], off
	global_load_dwordx4 v[208:211], v[60:61], off
	s_waitcnt vmcnt(16)
	v_mfma_f32_16x16x32_bf16 v[132:135], v[212:215], v[216:219], v[132:135]
	s_waitcnt vmcnt(15)
	v_mfma_f32_16x16x32_bf16 v[136:139], v[212:215], v[220:223], v[136:139]
	s_waitcnt vmcnt(14)
	v_mfma_f32_16x16x32_bf16 v[140:143], v[212:215], v[224:227], v[140:143]
	s_waitcnt vmcnt(13)
	v_mfma_f32_16x16x32_bf16 v[144:147], v[212:215], v[228:231], v[144:147]
	s_waitcnt vmcnt(12)
	v_mfma_f32_16x16x32_bf16 v[160:163], v[212:215], v[232:235], v[160:163]
	s_waitcnt vmcnt(11)
	v_mfma_f32_16x16x32_bf16 v[164:167], v[212:215], v[236:239], v[164:167]
	s_waitcnt vmcnt(10)
	v_mfma_f32_16x16x32_bf16 v[168:171], v[212:215], v[240:243], v[168:171]
	s_waitcnt vmcnt(9)
	v_mfma_f32_16x16x32_bf16 v[128:131], v[212:215], v[244:247], v[128:131]
	s_waitcnt vmcnt(7)
	v_mfma_f32_16x16x32_bf16 v[132:135], v[176:179], v[180:183], v[132:135]
	s_waitcnt vmcnt(6)
	v_mfma_f32_16x16x32_bf16 v[136:139], v[176:179], v[184:187], v[136:139]
	s_waitcnt vmcnt(5)
	v_mfma_f32_16x16x32_bf16 v[140:143], v[176:179], v[188:191], v[140:143]
	s_waitcnt vmcnt(4)
	v_mfma_f32_16x16x32_bf16 v[144:147], v[176:179], v[192:195], v[144:147]
	s_waitcnt vmcnt(3)
	v_mfma_f32_16x16x32_bf16 v[160:163], v[176:179], v[196:199], v[160:163]
	s_waitcnt vmcnt(2)
	v_mfma_f32_16x16x32_bf16 v[164:167], v[176:179], v[200:203], v[164:167]
	s_waitcnt vmcnt(1)
	v_mfma_f32_16x16x32_bf16 v[168:171], v[176:179], v[204:207], v[168:171]
	s_waitcnt vmcnt(0)
; __device__ __forceinline__ void p11_route(Frame& F) {
;     ...
;             for (int ks = 0; ks < 4; ++ks) { const gbf16x8 a = *(const gbf16x8*)(QRY + (size_t)(t0 + l15) * 2048 + h * 256 + c * 128 + 32 * ks + 8 * g);
; #pragma unroll
;                 for (int nt = 0; nt < 8; ++nt) acc[nt] = __builtin_amdgcn_mfma_f32_16x16x32_bf16(a, *(const gbf16x8*)(SK + ((size_t)(h * 2 + c) * PNK + 16 * nt + l15) * 128 + 32 * ks + 8 * g), acc[nt], 0, 0, 0); }
; #pragma unroll
;             for (int nt = 0; nt < 8; ++nt)
; #pragma unroll
;                 for (int r = 0; r < 4; ++r) sc[(c * 16 + 4 * g + r) * 129 + 16 * nt + l15] = acc[nt][r];
	v_mfma_f32_16x16x32_bf16 v[128:131], v[176:179], v[208:211], v[128:131]
	s_nop 3
	ds_write2_b32 v151, v132, v136 offset1:16
	ds_write2_b32 v151, v133, v137 offset0:129 offset1:145
	v_add_u32_e32 v132, 0x400, v151
	ds_write2_b32 v132, v134, v138 offset0:2 offset1:18
	ds_write2_b32 v132, v135, v139 offset0:131 offset1:147
	ds_write2_b32 v151, v140, v144 offset0:32 offset1:48
	ds_write2_b32 v151, v141, v145 offset0:161 offset1:177
	ds_write2_b32 v132, v142, v146 offset0:34 offset1:50
	ds_write2_b32 v132, v143, v147 offset0:163 offset1:179
	ds_write2_b32 v151, v160, v164 offset0:64 offset1:80
	ds_write2_b32 v151, v161, v165 offset0:193 offset1:209
	ds_write2_b32 v132, v162, v166 offset0:66 offset1:82
	ds_write2_b32 v132, v163, v167 offset0:195 offset1:211
	ds_write2_b32 v151, v168, v128 offset0:96 offset1:112
	ds_write2_b32 v151, v169, v129 offset0:225 offset1:241
	ds_write2_b32 v132, v170, v130 offset0:98 offset1:114
	ds_write2_b32 v132, v171, v131 offset0:227 offset1:243
	global_load_dwordx4 v[128:131], v[126:127], off offset:256
	global_load_dwordx4 v[132:135], v[62:63], off
	global_load_dwordx4 v[136:139], v[64:65], off
	global_load_dwordx4 v[140:143], v[66:67], off
	global_load_dwordx4 v[144:147], v[68:69], off
	global_load_dwordx4 v[160:163], v[70:71], off
	global_load_dwordx4 v[164:167], v[72:73], off
	global_load_dwordx4 v[168:171], v[74:75], off
	global_load_dwordx4 v[172:175], v[76:77], off
	global_load_dwordx4 v[176:179], v[126:127], off offset:320
	global_load_dwordx4 v[180:183], v[78:79], off
	global_load_dwordx4 v[184:187], v[80:81], off
	global_load_dwordx4 v[188:191], v[82:83], off
	global_load_dwordx4 v[192:195], v[84:85], off
	global_load_dwordx4 v[196:199], v[86:87], off
	global_load_dwordx4 v[200:203], v[88:89], off
	global_load_dwordx4 v[204:207], v[90:91], off
	global_load_dwordx4 v[208:211], v[92:93], off
	global_load_dwordx4 v[212:215], v[126:127], off offset:384
	global_load_dwordx4 v[216:219], v[94:95], off
	global_load_dwordx4 v[220:223], v[96:97], off
	global_load_dwordx4 v[224:227], v[98:99], off
	global_load_dwordx4 v[228:231], v[100:101], off
	global_load_dwordx4 v[232:235], v[102:103], off
	global_load_dwordx4 v[236:239], v[104:105], off
	global_load_dwordx4 v[240:243], v[106:107], off
	global_load_dwordx4 v[244:247], v[108:109], off
	s_waitcnt vmcnt(25)
	v_mfma_f32_16x16x32_bf16 v[132:135], v[128:131], v[132:135], 0
	s_waitcnt vmcnt(24)
	v_mfma_f32_16x16x32_bf16 v[136:139], v[128:131], v[136:139], 0
	s_waitcnt vmcnt(23)
	v_mfma_f32_16x16x32_bf16 v[140:143], v[128:131], v[140:143], 0
	s_waitcnt vmcnt(22)
	v_mfma_f32_16x16x32_bf16 v[144:147], v[128:131], v[144:147], 0
	s_waitcnt vmcnt(21)
	v_mfma_f32_16x16x32_bf16 v[160:163], v[128:131], v[160:163], 0
	s_waitcnt vmcnt(20)
	v_mfma_f32_16x16x32_bf16 v[164:167], v[128:131], v[164:167], 0
	s_waitcnt vmcnt(19)
	v_mfma_f32_16x16x32_bf16 v[168:171], v[128:131], v[168:171], 0
	s_waitcnt vmcnt(18)
	v_mfma_f32_16x16x32_bf16 v[128:131], v[128:131], v[172:175], 0
	s_waitcnt vmcnt(16)
	v_mfma_f32_16x16x32_bf16 v[132:135], v[176:179], v[180:183], v[132:135]
	s_waitcnt vmcnt(15)
	v_mfma_f32_16x16x32_bf16 v[136:139], v[176:179], v[184:187], v[136:139]
	s_waitcnt vmcnt(14)
	v_mfma_f32_16x16x32_bf16 v[140:143], v[176:179], v[188:191], v[140:143]
	s_waitcnt vmcnt(13)
	v_mfma_f32_16x16x32_bf16 v[144:147], v[176:179], v[192:195], v[144:147]
	s_waitcnt vmcnt(12)
	v_mfma_f32_16x16x32_bf16 v[160:163], v[176:179], v[196:199], v[160:163]
	s_waitcnt vmcnt(11)
	v_mfma_f32_16x16x32_bf16 v[164:167], v[176:179], v[200:203], v[164:167]
	s_waitcnt vmcnt(10)
	v_mfma_f32_16x16x32_bf16 v[168:171], v[176:179], v[204:207], v[168:171]
	s_waitcnt vmcnt(9)
	v_mfma_f32_16x16x32_bf16 v[128:131], v[176:179], v[208:211], v[128:131]
	global_load_dwordx4 v[176:179], v[126:127], off offset:448
	global_load_dwordx4 v[180:183], v[110:111], off
	global_load_dwordx4 v[184:187], v[112:113], off
	global_load_dwordx4 v[188:191], v[114:115], off
	global_load_dwordx4 v[192:195], v[116:117], off
	global_load_dwordx4 v[196:199], v[118:119], off
	global_load_dwordx4 v[200:203], v[120:121], off
	global_load_dwordx4 v[204:207], v[122:123], off
	global_load_dwordx4 v[208:211], v[124:125], off
	s_waitcnt vmcnt(16)
	v_mfma_f32_16x16x32_bf16 v[132:135], v[212:215], v[216:219], v[132:135]
	s_waitcnt vmcnt(15)
	v_mfma_f32_16x16x32_bf16 v[136:139], v[212:215], v[220:223], v[136:139]
	s_waitcnt vmcnt(14)
	v_mfma_f32_16x16x32_bf16 v[140:143], v[212:215], v[224:227], v[140:143]
	s_waitcnt vmcnt(13)
	v_mfma_f32_16x16x32_bf16 v[144:147], v[212:215], v[228:231], v[144:147]
	s_waitcnt vmcnt(12)
	v_mfma_f32_16x16x32_bf16 v[160:163], v[212:215], v[232:235], v[160:163]
	s_waitcnt vmcnt(11)
	v_mfma_f32_16x16x32_bf16 v[164:167], v[212:215], v[236:239], v[164:167]
	s_waitcnt vmcnt(10)
	v_mfma_f32_16x16x32_bf16 v[168:171], v[212:215], v[240:243], v[168:171]
	s_waitcnt vmcnt(9)
	v_mfma_f32_16x16x32_bf16 v[128:131], v[212:215], v[244:247], v[128:131]
	s_waitcnt vmcnt(7)
	v_mfma_f32_16x16x32_bf16 v[132:135], v[176:179], v[180:183], v[132:135]
	s_waitcnt vmcnt(6)
	v_mfma_f32_16x16x32_bf16 v[136:139], v[176:179], v[184:187], v[136:139]
	s_waitcnt vmcnt(5)
	v_mfma_f32_16x16x32_bf16 v[140:143], v[176:179], v[188:191], v[140:143]
	s_waitcnt vmcnt(4)
	v_mfma_f32_16x16x32_bf16 v[144:147], v[176:179], v[192:195], v[144:147]
	s_waitcnt vmcnt(3)
	v_mfma_f32_16x16x32_bf16 v[160:163], v[176:179], v[196:199], v[160:163]
	s_waitcnt vmcnt(2)
	v_mfma_f32_16x16x32_bf16 v[164:167], v[176:179], v[200:203], v[164:167]
	s_waitcnt vmcnt(1)
	v_mfma_f32_16x16x32_bf16 v[168:171], v[176:179], v[204:207], v[168:171]
	s_waitcnt vmcnt(0)
; #define LAS __attribute__((address_space(3)))
; __device__ __forceinline__ float uniq_key(float s, int n) { return __uint_as_float((__float_as_uint(s) & ~0xffu) | (unsigned)(255 - n)); }
; #define INS16(A_, X_) do { float x_ = (X_); _Pragma("unroll") for (int i_ = 0; i_ < 16; ++i_) { const float hi_ = fmaxf(A_[i_], x_); x_ = fminf(A_[i_], x_); A_[i_] = hi_; } } while (0)
; __device__ __forceinline__ void p11_route(Frame& F) {
;     ...
;                 for (int r = 0; r < 4; ++r) sc[(c * 16 + 4 * g + r) * 129 + 16 * nt + l15] = acc[nt][r];
;         }
;         { LAS float* row = sc + (F.lane & 31) * 129; float a[16]; const int nb = (F.lane >> 5) * (PNK / 2);
; #pragma unroll
;             for (int i = 0; i < 16; ++i) a[i] = -INFINITY;
; #pragma unroll 4
;             for (int n = 0; n < PNK / 2; ++n) INS16(a, uniq_key(row[nb + n], nb + n));
	v_mfma_f32_16x16x32_bf16 v[126:129], v[176:179], v[208:211], v[128:131]
	s_nop 2
	v_add_u32_e32 v130, 0x2000, v151
	v_add_u32_e32 v131, 0x2400, v151
	ds_write2_b32 v130, v132, v136 offset0:16 offset1:32
	ds_write2_b32 v130, v133, v137 offset0:145 offset1:161
	ds_write2_b32 v131, v134, v138 offset0:18 offset1:34
	ds_write2_b32 v131, v135, v139 offset0:147 offset1:163
	ds_write2_b32 v130, v140, v144 offset0:48 offset1:64
	ds_write2_b32 v130, v141, v145 offset0:177 offset1:193
	ds_write2_b32 v131, v142, v146 offset0:50 offset1:66
	ds_write2_b32 v131, v143, v147 offset0:179 offset1:195
	ds_write2_b32 v130, v160, v164 offset0:80 offset1:96
	ds_write2_b32 v130, v161, v165 offset0:209 offset1:225
	ds_write2_b32 v131, v162, v166 offset0:82 offset1:98
	ds_write2_b32 v131, v163, v167 offset0:211 offset1:227
	ds_write2_b32 v130, v168, v126 offset0:112 offset1:128
	v_add_u32_e32 v126, 0x2200, v151
	ds_write2_b32 v126, v169, v127 offset0:113 offset1:129
	ds_write2_b32 v131, v170, v128 offset0:114 offset1:130
	v_add_u32_e32 v126, 0x2600, v151
	ds_write2_b32 v126, v171, v129 offset0:115 offset1:131
	ds_read2_b32 v[222:223], v155 offset0:0 offset1:1
	ds_read2_b32 v[224:225], v155 offset0:2 offset1:3
	ds_read2_b32 v[226:227], v155 offset0:4 offset1:5
	ds_read2_b32 v[228:229], v155 offset0:6 offset1:7
	ds_read2_b32 v[230:231], v155 offset0:8 offset1:9
	ds_read2_b32 v[232:233], v155 offset0:10 offset1:11
	ds_read2_b32 v[234:235], v155 offset0:12 offset1:13
	ds_read2_b32 v[236:237], v155 offset0:14 offset1:15
	s_waitcnt lgkmcnt(0)
	ds_read2_b32 v[238:239], v155 offset0:16 offset1:17
	ds_read2_b32 v[240:241], v155 offset0:18 offset1:19
	ds_read2_b32 v[242:243], v155 offset0:20 offset1:21
	ds_read2_b32 v[244:245], v155 offset0:22 offset1:23
	ds_read2_b32 v[246:247], v155 offset0:24 offset1:25
	ds_read2_b32 v[248:249], v155 offset0:26 offset1:27
	ds_read2_b32 v[250:251], v155 offset0:28 offset1:29
	ds_read2_b32 v[252:253], v155 offset0:30 offset1:31
	v_add_u32_e32 v127, 3, v156
	v_and_or_b32 v222, v222, s14, v127
	v_add_u32_e32 v130, 2, v156
	v_and_or_b32 v223, v223, s14, v130
	v_add_u32_e32 v127, 1, v156
	v_and_or_b32 v224, v224, s14, v127
	v_add_u32_e32 v130, 0, v156
	v_and_or_b32 v225, v225, s14, v130
	v_add_u32_e32 v127, -1, v156
	v_and_or_b32 v226, v226, s14, v127
	v_add_u32_e32 v130, -2, v156
	v_and_or_b32 v227, v227, s14, v130
	v_add_u32_e32 v127, -3, v156
	v_and_or_b32 v228, v228, s14, v127
	v_add_u32_e32 v130, -4, v156
	v_and_or_b32 v229, v229, s14, v130
	v_add_u32_e32 v127, -5, v156
	v_and_or_b32 v230, v230, s14, v127
	v_add_u32_e32 v130, -6, v156
	v_and_or_b32 v231, v231, s14, v130
	v_add_u32_e32 v127, -7, v156
	v_and_or_b32 v232, v232, s14, v127
	v_add_u32_e32 v130, -8, v156
	v_and_or_b32 v233, v233, s14, v130
	v_add_u32_e32 v127, -9, v156
	v_and_or_b32 v234, v234, s14, v127
	v_add_u32_e32 v130, -10, v156
	v_and_or_b32 v235, v235, s14, v130
	v_add_u32_e32 v127, -11, v156
	v_and_or_b32 v236, v236, s14, v127
	v_add_u32_e32 v130, -12, v156
	v_and_or_b32 v237, v237, s14, v130
	v_max_f32_e32 v254, v222, v223
	v_min_f32_e32 v223, v222, v223
	v_max_f32_e32 v222, v224, v225
	v_min_f32_e32 v225, v224, v225
	v_max_f32_e32 v224, v254, v222
	v_min_f32_e32 v222, v254, v222
	v_max_f32_e32 v254, v223, v225
	v_min_f32_e32 v225, v223, v225
	v_max_f32_e32 v223, v254, v222
	v_min_f32_e32 v222, v254, v222
	v_max_f32_e32 v254, v226, v227
	v_min_f32_e32 v227, v226, v227
	v_max_f32_e32 v226, v228, v229
	v_min_f32_e32 v229, v228, v229
	v_max_f32_e32 v228, v254, v226
	v_min_f32_e32 v226, v254, v226
	v_max_f32_e32 v254, v227, v229
	v_min_f32_e32 v229, v227, v229
	v_max_f32_e32 v227, v254, v226
	v_min_f32_e32 v226, v254, v226
	v_max_f32_e32 v254, v224, v228
	v_min_f32_e32 v228, v224, v228
	v_max_f32_e32 v224, v222, v226
	v_min_f32_e32 v226, v222, v226
	v_max_f32_e32 v222, v224, v228
	v_min_f32_e32 v228, v224, v228
	v_max_f32_e32 v224, v223, v227
	v_min_f32_e32 v227, v223, v227
	v_max_f32_e32 v223, v225, v229
	v_min_f32_e32 v229, v225, v229
	v_max_f32_e32 v225, v223, v227
	v_min_f32_e32 v227, v223, v227
	v_max_f32_e32 v223, v224, v222
	v_min_f32_e32 v222, v224, v222
	v_max_f32_e32 v224, v225, v228
	v_min_f32_e32 v228, v225, v228
	v_max_f32_e32 v225, v227, v226
	v_min_f32_e32 v226, v227, v226
	v_max_f32_e32 v227, v230, v231
	v_min_f32_e32 v231, v230, v231
	v_max_f32_e32 v230, v232, v233
	v_min_f32_e32 v233, v232, v233
	v_max_f32_e32 v232, v227, v230
	v_min_f32_e32 v230, v227, v230
	v_max_f32_e32 v227, v231, v233
	v_min_f32_e32 v233, v231, v233
	v_max_f32_e32 v231, v227, v230
	v_min_f32_e32 v230, v227, v230
	v_max_f32_e32 v227, v234, v235
	v_min_f32_e32 v235, v234, v235
	v_max_f32_e32 v234, v236, v237
	v_min_f32_e32 v237, v236, v237
	v_max_f32_e32 v236, v227, v234
	v_min_f32_e32 v234, v227, v234
	v_max_f32_e32 v227, v235, v237
	v_min_f32_e32 v237, v235, v237
	v_max_f32_e32 v235, v227, v234
	v_min_f32_e32 v234, v227, v234
	v_max_f32_e32 v227, v232, v236
	v_min_f32_e32 v236, v232, v236
	v_max_f32_e32 v232, v230, v234
	v_min_f32_e32 v234, v230, v234
	v_max_f32_e32 v230, v232, v236
	v_min_f32_e32 v236, v232, v236
	v_max_f32_e32 v232, v231, v235
	v_min_f32_e32 v235, v231, v235
	v_max_f32_e32 v231, v233, v237
	v_min_f32_e32 v237, v233, v237
	v_max_f32_e32 v233, v231, v235
	v_min_f32_e32 v235, v231, v235
	v_max_f32_e32 v231, v232, v230
	v_min_f32_e32 v230, v232, v230
	v_max_f32_e32 v232, v233, v236
	v_min_f32_e32 v236, v233, v236
	v_max_f32_e32 v233, v235, v234
	v_min_f32_e32 v234, v235, v234
	v_max_f32_e32 v235, v254, v227
	v_min_f32_e32 v227, v254, v227
	v_max_f32_e32 v254, v228, v236
	v_min_f32_e32 v236, v228, v236
	v_max_f32_e32 v228, v254, v227
	v_min_f32_e32 v227, v254, v227
; #define LAS __attribute__((address_space(3)))
; #define INS16(A_, X_) do { float x_ = (X_); _Pragma("unroll") for (int i_ = 0; i_ < 16; ++i_) { const float hi_ = fmaxf(A_[i_], x_); x_ = fminf(A_[i_], x_); A_[i_] = hi_; } } while (0)
; __device__ __forceinline__ float uniq_key(float s, int n) { return __uint_as_float((__float_as_uint(s) & ~0xffu) | (unsigned)(255 - n)); }
; __device__ __forceinline__ void p11_route(Frame& F) {
;     ...
;         { LAS float* row = sc + (F.lane & 31) * 129; float a[16]; const int nb = (F.lane >> 5) * (PNK / 2);
; #pragma unroll
;             for (int i = 0; i < 16; ++i) a[i] = -INFINITY;
; #pragma unroll 4
;             for (int n = 0; n < PNK / 2; ++n) INS16(a, uniq_key(row[nb + n], nb + n));
	v_max_f32_e32 v254, v222, v230
	v_min_f32_e32 v230, v222, v230
	v_max_f32_e32 v222, v226, v234
	v_min_f32_e32 v234, v226, v234
	v_max_f32_e32 v226, v222, v230
	v_min_f32_e32 v230, v222, v230
	v_max_f32_e32 v222, v254, v228
	v_min_f32_e32 v228, v254, v228
	v_max_f32_e32 v254, v226, v227
	v_min_f32_e32 v227, v226, v227
	v_max_f32_e32 v226, v230, v236
	v_min_f32_e32 v236, v230, v236
	v_max_f32_e32 v230, v223, v231
	v_min_f32_e32 v231, v223, v231
	v_max_f32_e32 v223, v225, v233
	v_min_f32_e32 v233, v225, v233
	v_max_f32_e32 v225, v223, v231
	v_min_f32_e32 v231, v223, v231
	v_max_f32_e32 v223, v224, v232
	v_min_f32_e32 v232, v224, v232
	v_max_f32_e32 v224, v229, v237
	v_min_f32_e32 v237, v229, v237
	v_max_f32_e32 v229, v224, v232
	v_min_f32_e32 v232, v224, v232
	v_max_f32_e32 v224, v223, v225
	v_min_f32_e32 v225, v223, v225
	v_max_f32_e32 v223, v229, v231
	v_min_f32_e32 v231, v229, v231
	v_max_f32_e32 v229, v232, v233
	v_min_f32_e32 v233, v232, v233
	v_max_f32_e32 v232, v230, v222
	v_min_f32_e32 v222, v230, v222
	v_max_f32_e32 v230, v224, v228
	v_min_f32_e32 v228, v224, v228
	v_max_f32_e32 v224, v225, v254
	v_min_f32_e32 v254, v225, v254
	v_max_f32_e32 v225, v223, v227
	v_min_f32_e32 v227, v223, v227
	v_max_f32_e32 v223, v231, v226
	v_min_f32_e32 v226, v231, v226
	v_max_f32_e32 v231, v229, v236
	v_min_f32_e32 v236, v229, v236
	v_max_f32_e32 v229, v233, v234
	v_min_f32_e32 v234, v233, v234
	s_waitcnt lgkmcnt(0)
	v_add_u32_e32 v127, -13, v156
	v_and_or_b32 v238, v238, s14, v127
	v_add_u32_e32 v130, -14, v156
	v_and_or_b32 v239, v239, s14, v130
	v_add_u32_e32 v127, -15, v156
	v_and_or_b32 v240, v240, s14, v127
	v_add_u32_e32 v130, -16, v156
	v_and_or_b32 v241, v241, s14, v130
	v_add_u32_e32 v127, 0xffffffef, v156
	v_and_or_b32 v242, v242, s14, v127
	v_add_u32_e32 v130, 0xffffffee, v156
	v_and_or_b32 v243, v243, s14, v130
	v_add_u32_e32 v127, 0xffffffed, v156
	v_and_or_b32 v244, v244, s14, v127
	v_add_u32_e32 v130, 0xffffffec, v156
	v_and_or_b32 v245, v245, s14, v130
	v_add_u32_e32 v127, 0xffffffeb, v156
	v_and_or_b32 v246, v246, s14, v127
	v_add_u32_e32 v130, 0xffffffea, v156
	v_and_or_b32 v247, v247, s14, v130
	v_add_u32_e32 v127, 0xffffffe9, v156
	v_and_or_b32 v248, v248, s14, v127
	v_add_u32_e32 v130, 0xffffffe8, v156
	v_and_or_b32 v249, v249, s14, v130
	v_add_u32_e32 v127, 0xffffffe7, v156
	v_and_or_b32 v250, v250, s14, v127
	v_add_u32_e32 v130, 0xffffffe6, v156
	v_and_or_b32 v251, v251, s14, v130
	v_add_u32_e32 v127, 0xffffffe5, v156
	v_and_or_b32 v252, v252, s14, v127
	v_add_u32_e32 v130, 0xffffffe4, v156
	v_and_or_b32 v253, v253, s14, v130
	v_max_f32_e32 v128, v238, v239
	v_min_f32_e32 v239, v238, v239
	v_max_f32_e32 v238, v240, v241
	v_min_f32_e32 v241, v240, v241
	v_max_f32_e32 v240, v128, v238
	v_min_f32_e32 v238, v128, v238
	v_max_f32_e32 v128, v239, v241
	v_min_f32_e32 v241, v239, v241
	v_max_f32_e32 v239, v128, v238
	v_min_f32_e32 v238, v128, v238
	v_max_f32_e32 v128, v242, v243
	v_min_f32_e32 v243, v242, v243
	v_max_f32_e32 v242, v244, v245
	v_min_f32_e32 v245, v244, v245
	v_max_f32_e32 v244, v128, v242
	v_min_f32_e32 v242, v128, v242
	v_max_f32_e32 v128, v243, v245
	v_min_f32_e32 v245, v243, v245
	v_max_f32_e32 v243, v128, v242
	v_min_f32_e32 v242, v128, v242
	v_max_f32_e32 v128, v240, v244
	v_min_f32_e32 v244, v240, v244
	v_max_f32_e32 v240, v238, v242
	v_min_f32_e32 v242, v238, v242
	v_max_f32_e32 v238, v240, v244
	v_min_f32_e32 v244, v240, v244
	v_max_f32_e32 v240, v239, v243
	v_min_f32_e32 v243, v239, v243
	v_max_f32_e32 v239, v241, v245
	v_min_f32_e32 v245, v241, v245
	v_max_f32_e32 v241, v239, v243
	v_min_f32_e32 v243, v239, v243
	v_max_f32_e32 v239, v240, v238
	v_min_f32_e32 v238, v240, v238
	v_max_f32_e32 v240, v241, v244
	v_min_f32_e32 v244, v241, v244
	v_max_f32_e32 v241, v243, v242
	v_min_f32_e32 v242, v243, v242
	v_max_f32_e32 v243, v246, v247
	v_min_f32_e32 v247, v246, v247
	v_max_f32_e32 v246, v248, v249
	v_min_f32_e32 v249, v248, v249
	v_max_f32_e32 v248, v243, v246
	v_min_f32_e32 v246, v243, v246
	v_max_f32_e32 v243, v247, v249
	v_min_f32_e32 v249, v247, v249
	v_max_f32_e32 v247, v243, v246
	v_min_f32_e32 v246, v243, v246
	v_max_f32_e32 v243, v250, v251
	v_min_f32_e32 v251, v250, v251
	v_max_f32_e32 v250, v252, v253
	v_min_f32_e32 v253, v252, v253
	v_max_f32_e32 v252, v243, v250
	v_min_f32_e32 v250, v243, v250
	v_max_f32_e32 v243, v251, v253
	v_min_f32_e32 v253, v251, v253
	v_max_f32_e32 v251, v243, v250
	v_min_f32_e32 v250, v243, v250
	v_max_f32_e32 v243, v248, v252
	v_min_f32_e32 v252, v248, v252
	v_max_f32_e32 v248, v246, v250
	v_min_f32_e32 v250, v246, v250
	v_max_f32_e32 v246, v248, v252
	v_min_f32_e32 v252, v248, v252
	v_max_f32_e32 v248, v247, v251
	v_min_f32_e32 v251, v247, v251
	v_max_f32_e32 v247, v249, v253
	v_min_f32_e32 v253, v249, v253
	v_max_f32_e32 v249, v247, v251
	v_min_f32_e32 v251, v247, v251
	v_max_f32_e32 v247, v248, v246
	v_min_f32_e32 v246, v248, v246
	v_max_f32_e32 v248, v249, v252
	v_min_f32_e32 v252, v249, v252
	v_max_f32_e32 v249, v251, v250
	v_min_f32_e32 v250, v251, v250
	v_max_f32_e32 v251, v128, v243
	v_min_f32_e32 v243, v128, v243
	v_max_f32_e32 v128, v244, v252
	v_min_f32_e32 v252, v244, v252
	v_max_f32_e32 v244, v128, v243
	v_min_f32_e32 v243, v128, v243
	v_max_f32_e32 v128, v238, v246
	v_min_f32_e32 v246, v238, v246
	v_max_f32_e32 v238, v242, v250
	v_min_f32_e32 v250, v242, v250
	v_max_f32_e32 v242, v238, v246
	v_min_f32_e32 v246, v238, v246
	v_max_f32_e32 v238, v128, v244
	v_min_f32_e32 v244, v128, v244
	v_max_f32_e32 v128, v242, v243
	v_min_f32_e32 v243, v242, v243
	v_max_f32_e32 v242, v246, v252
	v_min_f32_e32 v252, v246, v252
	v_max_f32_e32 v246, v239, v247
; #define LAS __attribute__((address_space(3)))
; #define INS16(A_, X_) do { float x_ = (X_); _Pragma("unroll") for (int i_ = 0; i_ < 16; ++i_) { const float hi_ = fmaxf(A_[i_], x_); x_ = fminf(A_[i_], x_); A_[i_] = hi_; } } while (0)
; __device__ __forceinline__ float uniq_key(float s, int n) { return __uint_as_float((__float_as_uint(s) & ~0xffu) | (unsigned)(255 - n)); }
; __device__ __forceinline__ void p11_route(Frame& F) {
;     ...
;         { LAS float* row = sc + (F.lane & 31) * 129; float a[16]; const int nb = (F.lane >> 5) * (PNK / 2);
; #pragma unroll
;             for (int i = 0; i < 16; ++i) a[i] = -INFINITY;
; #pragma unroll 4
;             for (int n = 0; n < PNK / 2; ++n) INS16(a, uniq_key(row[nb + n], nb + n));
	v_min_f32_e32 v247, v239, v247
	v_max_f32_e32 v239, v241, v249
	v_min_f32_e32 v249, v241, v249
	v_max_f32_e32 v241, v239, v247
	v_min_f32_e32 v247, v239, v247
	v_max_f32_e32 v239, v240, v248
	v_min_f32_e32 v248, v240, v248
	v_max_f32_e32 v240, v245, v253
	v_min_f32_e32 v253, v245, v253
	v_max_f32_e32 v245, v240, v248
	v_min_f32_e32 v248, v240, v248
	v_max_f32_e32 v240, v239, v241
	v_min_f32_e32 v241, v239, v241
	v_max_f32_e32 v239, v245, v247
	v_min_f32_e32 v247, v245, v247
	v_max_f32_e32 v245, v248, v249
	v_min_f32_e32 v249, v248, v249
	v_max_f32_e32 v248, v246, v238
	v_min_f32_e32 v238, v246, v238
	v_max_f32_e32 v246, v240, v244
	v_min_f32_e32 v244, v240, v244
	v_max_f32_e32 v240, v241, v128
	v_min_f32_e32 v128, v241, v128
	v_max_f32_e32 v241, v239, v243
	v_min_f32_e32 v243, v239, v243
	v_max_f32_e32 v239, v247, v242
	v_min_f32_e32 v242, v247, v242
	v_max_f32_e32 v247, v245, v252
	v_min_f32_e32 v252, v245, v252
	v_max_f32_e32 v245, v249, v250
	v_min_f32_e32 v250, v249, v250
	v_max_f32_e32 v235, v235, v253
	v_max_f32_e32 v232, v232, v250
	v_max_f32_e32 v222, v222, v245
	v_max_f32_e32 v230, v230, v252
	v_max_f32_e32 v228, v228, v247
	v_max_f32_e32 v224, v224, v242
	v_max_f32_e32 v254, v254, v239
	v_max_f32_e32 v225, v225, v243
	v_max_f32_e32 v227, v227, v241
	v_max_f32_e32 v223, v223, v128
	v_max_f32_e32 v226, v226, v240
	v_max_f32_e32 v231, v231, v244
	v_max_f32_e32 v236, v236, v246
	v_max_f32_e32 v229, v229, v238
	v_max_f32_e32 v234, v234, v248
	v_max_f32_e32 v237, v237, v251
	ds_read2_b32 v[238:239], v155 offset0:32 offset1:33
	ds_read2_b32 v[240:241], v155 offset0:34 offset1:35
	ds_read2_b32 v[242:243], v155 offset0:36 offset1:37
	ds_read2_b32 v[244:245], v155 offset0:38 offset1:39
	ds_read2_b32 v[246:247], v155 offset0:40 offset1:41
	ds_read2_b32 v[248:249], v155 offset0:42 offset1:43
	ds_read2_b32 v[250:251], v155 offset0:44 offset1:45
	ds_read2_b32 v[252:253], v155 offset0:46 offset1:47
	v_max_f32_e32 v233, v235, v227
	v_min_f32_e32 v227, v235, v227
	v_max_f32_e32 v235, v232, v223
	v_min_f32_e32 v223, v232, v223
	v_max_f32_e32 v232, v222, v226
	v_min_f32_e32 v226, v222, v226
	v_max_f32_e32 v222, v230, v231
	v_min_f32_e32 v231, v230, v231
	v_max_f32_e32 v230, v228, v236
	v_min_f32_e32 v236, v228, v236
	v_max_f32_e32 v228, v224, v229
	v_min_f32_e32 v229, v224, v229
	v_max_f32_e32 v224, v254, v234
	v_min_f32_e32 v234, v254, v234
	v_max_f32_e32 v254, v225, v237
	v_min_f32_e32 v237, v225, v237
	v_max_f32_e32 v225, v233, v230
	v_min_f32_e32 v230, v233, v230
	v_max_f32_e32 v233, v235, v228
	v_min_f32_e32 v228, v235, v228
	v_max_f32_e32 v235, v232, v224
	v_min_f32_e32 v224, v232, v224
	v_max_f32_e32 v232, v222, v254
	v_min_f32_e32 v254, v222, v254
	v_max_f32_e32 v222, v227, v236
	v_min_f32_e32 v236, v227, v236
	v_max_f32_e32 v227, v223, v229
	v_min_f32_e32 v229, v223, v229
	v_max_f32_e32 v223, v226, v234
	v_min_f32_e32 v234, v226, v234
	v_max_f32_e32 v226, v231, v237
	v_min_f32_e32 v237, v231, v237
	v_max_f32_e32 v231, v225, v235
	v_min_f32_e32 v235, v225, v235
	v_max_f32_e32 v225, v233, v232
	v_min_f32_e32 v232, v233, v232
	v_max_f32_e32 v233, v230, v224
	v_min_f32_e32 v224, v230, v224
	v_max_f32_e32 v230, v228, v254
	v_min_f32_e32 v254, v228, v254
	v_max_f32_e32 v228, v222, v223
	v_min_f32_e32 v223, v222, v223
	v_max_f32_e32 v222, v227, v226
	v_min_f32_e32 v226, v227, v226
	v_max_f32_e32 v227, v236, v234
	v_min_f32_e32 v234, v236, v234
	v_max_f32_e32 v236, v229, v237
	v_min_f32_e32 v237, v229, v237
	v_max_f32_e32 v229, v231, v225
	v_min_f32_e32 v225, v231, v225
	v_max_f32_e32 v231, v235, v232
	v_min_f32_e32 v232, v235, v232
	v_max_f32_e32 v235, v233, v230
	v_min_f32_e32 v230, v233, v230
	v_max_f32_e32 v233, v224, v254
	v_min_f32_e32 v254, v224, v254
	v_max_f32_e32 v224, v228, v222
	v_min_f32_e32 v222, v228, v222
	v_max_f32_e32 v228, v223, v226
	v_min_f32_e32 v226, v223, v226
	v_max_f32_e32 v223, v227, v236
	v_min_f32_e32 v236, v227, v236
	v_max_f32_e32 v227, v234, v237
	v_min_f32_e32 v237, v234, v237
	s_waitcnt lgkmcnt(0)
	v_add_u32_e32 v127, 0xffffffe3, v156
	v_and_or_b32 v238, v238, s14, v127
	v_add_u32_e32 v130, 0xffffffe2, v156
	v_and_or_b32 v239, v239, s14, v130
	v_add_u32_e32 v127, 0xffffffe1, v156
	v_and_or_b32 v240, v240, s14, v127
	v_add_u32_e32 v130, 0xffffffe0, v156
	v_and_or_b32 v241, v241, s14, v130
	v_add_u32_e32 v127, 0xffffffdf, v156
	v_and_or_b32 v242, v242, s14, v127
	v_add_u32_e32 v130, 0xffffffde, v156
	v_and_or_b32 v243, v243, s14, v130
	v_add_u32_e32 v127, 0xffffffdd, v156
	v_and_or_b32 v244, v244, s14, v127
	v_add_u32_e32 v130, 0xffffffdc, v156
	v_and_or_b32 v245, v245, s14, v130
	v_add_u32_e32 v127, 0xffffffdb, v156
	v_and_or_b32 v246, v246, s14, v127
	v_add_u32_e32 v130, 0xffffffda, v156
	v_and_or_b32 v247, v247, s14, v130
	v_add_u32_e32 v127, 0xffffffd9, v156
	v_and_or_b32 v248, v248, s14, v127
	v_add_u32_e32 v130, 0xffffffd8, v156
	v_and_or_b32 v249, v249, s14, v130
	v_add_u32_e32 v127, 0xffffffd7, v156
	v_and_or_b32 v250, v250, s14, v127
	v_add_u32_e32 v130, 0xffffffd6, v156
	v_and_or_b32 v251, v251, s14, v130
	v_add_u32_e32 v127, 0xffffffd5, v156
	v_and_or_b32 v252, v252, s14, v127
	v_add_u32_e32 v130, 0xffffffd4, v156
	v_and_or_b32 v253, v253, s14, v130
	v_max_f32_e32 v128, v238, v239
	v_min_f32_e32 v239, v238, v239
	v_max_f32_e32 v238, v240, v241
	v_min_f32_e32 v241, v240, v241
	v_max_f32_e32 v240, v128, v238
	v_min_f32_e32 v238, v128, v238
	v_max_f32_e32 v128, v239, v241
	v_min_f32_e32 v241, v239, v241
	v_max_f32_e32 v239, v128, v238
	v_min_f32_e32 v238, v128, v238
	v_max_f32_e32 v128, v242, v243
	v_min_f32_e32 v243, v242, v243
	v_max_f32_e32 v242, v244, v245
	v_min_f32_e32 v245, v244, v245
; #define LAS __attribute__((address_space(3)))
; #define INS16(A_, X_) do { float x_ = (X_); _Pragma("unroll") for (int i_ = 0; i_ < 16; ++i_) { const float hi_ = fmaxf(A_[i_], x_); x_ = fminf(A_[i_], x_); A_[i_] = hi_; } } while (0)
; __device__ __forceinline__ float uniq_key(float s, int n) { return __uint_as_float((__float_as_uint(s) & ~0xffu) | (unsigned)(255 - n)); }
; __device__ __forceinline__ void p11_route(Frame& F) {
;     ...
;         { LAS float* row = sc + (F.lane & 31) * 129; float a[16]; const int nb = (F.lane >> 5) * (PNK / 2);
; #pragma unroll
;             for (int i = 0; i < 16; ++i) a[i] = -INFINITY;
; #pragma unroll 4
;             for (int n = 0; n < PNK / 2; ++n) INS16(a, uniq_key(row[nb + n], nb + n));
	v_max_f32_e32 v244, v128, v242
	v_min_f32_e32 v242, v128, v242
	v_max_f32_e32 v128, v243, v245
	v_min_f32_e32 v245, v243, v245
	v_max_f32_e32 v243, v128, v242
	v_min_f32_e32 v242, v128, v242
	v_max_f32_e32 v128, v240, v244
	v_min_f32_e32 v244, v240, v244
	v_max_f32_e32 v240, v238, v242
	v_min_f32_e32 v242, v238, v242
	v_max_f32_e32 v238, v240, v244
	v_min_f32_e32 v244, v240, v244
	v_max_f32_e32 v240, v239, v243
	v_min_f32_e32 v243, v239, v243
	v_max_f32_e32 v239, v241, v245
	v_min_f32_e32 v245, v241, v245
	v_max_f32_e32 v241, v239, v243
	v_min_f32_e32 v243, v239, v243
	v_max_f32_e32 v239, v240, v238
	v_min_f32_e32 v238, v240, v238
	v_max_f32_e32 v240, v241, v244
	v_min_f32_e32 v244, v241, v244
	v_max_f32_e32 v241, v243, v242
	v_min_f32_e32 v242, v243, v242
	v_max_f32_e32 v243, v246, v247
	v_min_f32_e32 v247, v246, v247
	v_max_f32_e32 v246, v248, v249
	v_min_f32_e32 v249, v248, v249
	v_max_f32_e32 v248, v243, v246
	v_min_f32_e32 v246, v243, v246
	v_max_f32_e32 v243, v247, v249
	v_min_f32_e32 v249, v247, v249
	v_max_f32_e32 v247, v243, v246
	v_min_f32_e32 v246, v243, v246
	v_max_f32_e32 v243, v250, v251
	v_min_f32_e32 v251, v250, v251
	v_max_f32_e32 v250, v252, v253
	v_min_f32_e32 v253, v252, v253
	v_max_f32_e32 v252, v243, v250
	v_min_f32_e32 v250, v243, v250
	v_max_f32_e32 v243, v251, v253
	v_min_f32_e32 v253, v251, v253
	v_max_f32_e32 v251, v243, v250
	v_min_f32_e32 v250, v243, v250
	v_max_f32_e32 v243, v248, v252
	v_min_f32_e32 v252, v248, v252
	v_max_f32_e32 v248, v246, v250
	v_min_f32_e32 v250, v246, v250
	v_max_f32_e32 v246, v248, v252
	v_min_f32_e32 v252, v248, v252
	v_max_f32_e32 v248, v247, v251
	v_min_f32_e32 v251, v247, v251
	v_max_f32_e32 v247, v249, v253
	v_min_f32_e32 v253, v249, v253
	v_max_f32_e32 v249, v247, v251
	v_min_f32_e32 v251, v247, v251
	v_max_f32_e32 v247, v248, v246
	v_min_f32_e32 v246, v248, v246
	v_max_f32_e32 v248, v249, v252
	v_min_f32_e32 v252, v249, v252
	v_max_f32_e32 v249, v251, v250
	v_min_f32_e32 v250, v251, v250
	v_max_f32_e32 v251, v128, v243
	v_min_f32_e32 v243, v128, v243
	v_max_f32_e32 v128, v244, v252
	v_min_f32_e32 v252, v244, v252
	v_max_f32_e32 v244, v128, v243
	v_min_f32_e32 v243, v128, v243
	v_max_f32_e32 v128, v238, v246
	v_min_f32_e32 v246, v238, v246
	v_max_f32_e32 v238, v242, v250
	v_min_f32_e32 v250, v242, v250
	v_max_f32_e32 v242, v238, v246
	v_min_f32_e32 v246, v238, v246
	v_max_f32_e32 v238, v128, v244
	v_min_f32_e32 v244, v128, v244
	v_max_f32_e32 v128, v242, v243
	v_min_f32_e32 v243, v242, v243
	v_max_f32_e32 v242, v246, v252
	v_min_f32_e32 v252, v246, v252
	v_max_f32_e32 v246, v239, v247
	v_min_f32_e32 v247, v239, v247
	v_max_f32_e32 v239, v241, v249
	v_min_f32_e32 v249, v241, v249
	v_max_f32_e32 v241, v239, v247
	v_min_f32_e32 v247, v239, v247
	v_max_f32_e32 v239, v240, v248
	v_min_f32_e32 v248, v240, v248
	v_max_f32_e32 v240, v245, v253
	v_min_f32_e32 v253, v245, v253
	v_max_f32_e32 v245, v240, v248
	v_min_f32_e32 v248, v240, v248
	v_max_f32_e32 v240, v239, v241
	v_min_f32_e32 v241, v239, v241
	v_max_f32_e32 v239, v245, v247
	v_min_f32_e32 v247, v245, v247
	v_max_f32_e32 v245, v248, v249
	v_min_f32_e32 v249, v248, v249
	v_max_f32_e32 v248, v246, v238
	v_min_f32_e32 v238, v246, v238
	v_max_f32_e32 v246, v240, v244
	v_min_f32_e32 v244, v240, v244
	v_max_f32_e32 v240, v241, v128
	v_min_f32_e32 v128, v241, v128
	v_max_f32_e32 v241, v239, v243
	v_min_f32_e32 v243, v239, v243
	v_max_f32_e32 v239, v247, v242
	v_min_f32_e32 v242, v247, v242
	v_max_f32_e32 v247, v245, v252
	v_min_f32_e32 v252, v245, v252
	v_max_f32_e32 v245, v249, v250
	v_min_f32_e32 v250, v249, v250
	v_max_f32_e32 v229, v229, v253
	v_max_f32_e32 v225, v225, v250
	v_max_f32_e32 v231, v231, v245
	v_max_f32_e32 v232, v232, v252
	v_max_f32_e32 v235, v235, v247
	v_max_f32_e32 v230, v230, v242
	v_max_f32_e32 v233, v233, v239
	v_max_f32_e32 v254, v254, v243
	v_max_f32_e32 v224, v224, v241
	v_max_f32_e32 v222, v222, v128
	v_max_f32_e32 v228, v228, v240
	v_max_f32_e32 v226, v226, v244
	v_max_f32_e32 v223, v223, v246
	v_max_f32_e32 v236, v236, v238
	v_max_f32_e32 v227, v227, v248
	v_max_f32_e32 v237, v237, v251
	ds_read2_b32 v[238:239], v155 offset0:48 offset1:49
	ds_read2_b32 v[240:241], v155 offset0:50 offset1:51
	ds_read2_b32 v[242:243], v155 offset0:52 offset1:53
	ds_read2_b32 v[244:245], v155 offset0:54 offset1:55
	ds_read2_b32 v[246:247], v155 offset0:56 offset1:57
	ds_read2_b32 v[248:249], v155 offset0:58 offset1:59
	ds_read2_b32 v[250:251], v155 offset0:60 offset1:61
	ds_read2_b32 v[252:253], v155 offset0:62 offset1:63
	v_max_f32_e32 v234, v229, v224
	v_min_f32_e32 v224, v229, v224
	v_max_f32_e32 v229, v225, v222
	v_min_f32_e32 v222, v225, v222
	v_max_f32_e32 v225, v231, v228
	v_min_f32_e32 v228, v231, v228
	v_max_f32_e32 v231, v232, v226
	v_min_f32_e32 v226, v232, v226
	v_max_f32_e32 v232, v235, v223
	v_min_f32_e32 v223, v235, v223
	v_max_f32_e32 v235, v230, v236
	v_min_f32_e32 v236, v230, v236
	v_max_f32_e32 v230, v233, v227
	v_min_f32_e32 v227, v233, v227
	v_max_f32_e32 v233, v254, v237
	v_min_f32_e32 v237, v254, v237
	v_max_f32_e32 v254, v234, v232
	v_min_f32_e32 v232, v234, v232
	v_max_f32_e32 v234, v229, v235
	v_min_f32_e32 v235, v229, v235
	v_max_f32_e32 v229, v225, v230
	v_min_f32_e32 v230, v225, v230
	v_max_f32_e32 v225, v231, v233
	v_min_f32_e32 v233, v231, v233
	v_max_f32_e32 v231, v224, v223
	v_min_f32_e32 v223, v224, v223
	v_max_f32_e32 v224, v222, v236
	v_min_f32_e32 v236, v222, v236
	v_max_f32_e32 v222, v228, v227
	v_min_f32_e32 v227, v228, v227
	v_max_f32_e32 v228, v226, v237
	v_min_f32_e32 v237, v226, v237
	v_max_f32_e32 v226, v254, v229
	v_min_f32_e32 v229, v254, v229
	v_max_f32_e32 v254, v234, v225
	v_min_f32_e32 v225, v234, v225
	v_max_f32_e32 v234, v232, v230
	v_min_f32_e32 v230, v232, v230
	v_max_f32_e32 v232, v235, v233
	v_min_f32_e32 v233, v235, v233
	v_max_f32_e32 v235, v231, v222
	v_min_f32_e32 v222, v231, v222
	v_max_f32_e32 v231, v224, v228
	v_min_f32_e32 v228, v224, v228
	v_max_f32_e32 v224, v223, v227
	v_min_f32_e32 v227, v223, v227
	v_max_f32_e32 v223, v236, v237
	v_min_f32_e32 v237, v236, v237
	v_max_f32_e32 v236, v226, v254
	v_min_f32_e32 v254, v226, v254
	v_max_f32_e32 v226, v229, v225
	v_min_f32_e32 v225, v229, v225
	v_max_f32_e32 v229, v234, v232
	v_min_f32_e32 v232, v234, v232
	v_max_f32_e32 v234, v230, v233
	v_min_f32_e32 v233, v230, v233
	v_max_f32_e32 v230, v235, v231
	v_min_f32_e32 v231, v235, v231
	v_max_f32_e32 v235, v222, v228
	v_min_f32_e32 v228, v222, v228
	v_max_f32_e32 v222, v224, v223
	v_min_f32_e32 v223, v224, v223
	v_max_f32_e32 v224, v227, v237
	v_min_f32_e32 v237, v227, v237
	s_waitcnt lgkmcnt(0)
; #define LAS __attribute__((address_space(3)))
; #define INS16(A_, X_) do { float x_ = (X_); _Pragma("unroll") for (int i_ = 0; i_ < 16; ++i_) { const float hi_ = fmaxf(A_[i_], x_); x_ = fminf(A_[i_], x_); A_[i_] = hi_; } } while (0)
; __device__ __forceinline__ float uniq_key(float s, int n) { return __uint_as_float((__float_as_uint(s) & ~0xffu) | (unsigned)(255 - n)); }
; __device__ __forceinline__ void p11_route(Frame& F) {
;     ...
;         { LAS float* row = sc + (F.lane & 31) * 129; float a[16]; const int nb = (F.lane >> 5) * (PNK / 2);
; #pragma unroll
;             for (int i = 0; i < 16; ++i) a[i] = -INFINITY;
; #pragma unroll 4
;             for (int n = 0; n < PNK / 2; ++n) INS16(a, uniq_key(row[nb + n], nb + n));
	v_add_u32_e32 v127, 0xffffffd3, v156
	v_and_or_b32 v238, v238, s14, v127
	v_add_u32_e32 v130, 0xffffffd2, v156
	v_and_or_b32 v239, v239, s14, v130
	v_add_u32_e32 v127, 0xffffffd1, v156
	v_and_or_b32 v240, v240, s14, v127
	v_add_u32_e32 v130, 0xffffffd0, v156
	v_and_or_b32 v241, v241, s14, v130
	v_add_u32_e32 v127, 0xffffffcf, v156
	v_and_or_b32 v242, v242, s14, v127
	v_add_u32_e32 v130, 0xffffffce, v156
	v_and_or_b32 v243, v243, s14, v130
	v_add_u32_e32 v127, 0xffffffcd, v156
	v_and_or_b32 v244, v244, s14, v127
	v_add_u32_e32 v130, 0xffffffcc, v156
	v_and_or_b32 v245, v245, s14, v130
	v_add_u32_e32 v127, 0xffffffcb, v156
	v_and_or_b32 v246, v246, s14, v127
	v_add_u32_e32 v130, 0xffffffca, v156
	v_and_or_b32 v247, v247, s14, v130
	v_add_u32_e32 v127, 0xffffffc9, v156
	v_and_or_b32 v248, v248, s14, v127
	v_add_u32_e32 v130, 0xffffffc8, v156
	v_and_or_b32 v249, v249, s14, v130
	v_add_u32_e32 v127, 0xffffffc7, v156
	v_and_or_b32 v250, v250, s14, v127
	v_add_u32_e32 v130, 0xffffffc6, v156
	v_and_or_b32 v251, v251, s14, v130
	v_add_u32_e32 v127, 0xffffffc5, v156
	v_and_or_b32 v252, v252, s14, v127
	v_add_u32_e32 v130, 0xffffffc4, v156
	v_and_or_b32 v253, v253, s14, v130
	v_max_f32_e32 v128, v238, v239
	v_min_f32_e32 v239, v238, v239
	v_max_f32_e32 v238, v240, v241
	v_min_f32_e32 v241, v240, v241
	v_max_f32_e32 v240, v128, v238
	v_min_f32_e32 v238, v128, v238
	v_max_f32_e32 v128, v239, v241
	v_min_f32_e32 v241, v239, v241
	v_max_f32_e32 v239, v128, v238
	v_min_f32_e32 v238, v128, v238
	v_max_f32_e32 v128, v242, v243
	v_min_f32_e32 v243, v242, v243
	v_max_f32_e32 v242, v244, v245
	v_min_f32_e32 v245, v244, v245
	v_max_f32_e32 v244, v128, v242
	v_min_f32_e32 v242, v128, v242
	v_max_f32_e32 v128, v243, v245
	v_min_f32_e32 v245, v243, v245
	v_max_f32_e32 v243, v128, v242
	v_min_f32_e32 v242, v128, v242
	v_max_f32_e32 v128, v240, v244
	v_min_f32_e32 v244, v240, v244
	v_max_f32_e32 v240, v238, v242
	v_min_f32_e32 v242, v238, v242
	v_max_f32_e32 v238, v240, v244
	v_min_f32_e32 v244, v240, v244
	v_max_f32_e32 v240, v239, v243
	v_min_f32_e32 v243, v239, v243
	v_max_f32_e32 v239, v241, v245
	v_min_f32_e32 v245, v241, v245
	v_max_f32_e32 v241, v239, v243
	v_min_f32_e32 v243, v239, v243
	v_max_f32_e32 v239, v240, v238
	v_min_f32_e32 v238, v240, v238
	v_max_f32_e32 v240, v241, v244
	v_min_f32_e32 v244, v241, v244
	v_max_f32_e32 v241, v243, v242
	v_min_f32_e32 v242, v243, v242
	v_max_f32_e32 v243, v246, v247
	v_min_f32_e32 v247, v246, v247
	v_max_f32_e32 v246, v248, v249
	v_min_f32_e32 v249, v248, v249
	v_max_f32_e32 v248, v243, v246
	v_min_f32_e32 v246, v243, v246
	v_max_f32_e32 v243, v247, v249
	v_min_f32_e32 v249, v247, v249
	v_max_f32_e32 v247, v243, v246
	v_min_f32_e32 v246, v243, v246
	v_max_f32_e32 v243, v250, v251
	v_min_f32_e32 v251, v250, v251
	v_max_f32_e32 v250, v252, v253
	v_min_f32_e32 v253, v252, v253
	v_max_f32_e32 v252, v243, v250
	v_min_f32_e32 v250, v243, v250
	v_max_f32_e32 v243, v251, v253
	v_min_f32_e32 v253, v251, v253
	v_max_f32_e32 v251, v243, v250
	v_min_f32_e32 v250, v243, v250
	v_max_f32_e32 v243, v248, v252
	v_min_f32_e32 v252, v248, v252
	v_max_f32_e32 v248, v246, v250
	v_min_f32_e32 v250, v246, v250
	v_max_f32_e32 v246, v248, v252
	v_min_f32_e32 v252, v248, v252
	v_max_f32_e32 v248, v247, v251
	v_min_f32_e32 v251, v247, v251
	v_max_f32_e32 v247, v249, v253
	v_min_f32_e32 v253, v249, v253
	v_max_f32_e32 v249, v247, v251
	v_min_f32_e32 v251, v247, v251
	v_max_f32_e32 v247, v248, v246
	v_min_f32_e32 v246, v248, v246
	v_max_f32_e32 v248, v249, v252
	v_min_f32_e32 v252, v249, v252
	v_max_f32_e32 v249, v251, v250
	v_min_f32_e32 v250, v251, v250
	v_max_f32_e32 v251, v128, v243
	v_min_f32_e32 v243, v128, v243
	v_max_f32_e32 v128, v244, v252
	v_min_f32_e32 v252, v244, v252
	v_max_f32_e32 v244, v128, v243
	v_min_f32_e32 v243, v128, v243
	v_max_f32_e32 v128, v238, v246
	v_min_f32_e32 v246, v238, v246
	v_max_f32_e32 v238, v242, v250
	v_min_f32_e32 v250, v242, v250
	v_max_f32_e32 v242, v238, v246
	v_min_f32_e32 v246, v238, v246
	v_max_f32_e32 v238, v128, v244
	v_min_f32_e32 v244, v128, v244
	v_max_f32_e32 v128, v242, v243
	v_min_f32_e32 v243, v242, v243
	v_max_f32_e32 v242, v246, v252
	v_min_f32_e32 v252, v246, v252
	v_max_f32_e32 v246, v239, v247
	v_min_f32_e32 v247, v239, v247
	v_max_f32_e32 v239, v241, v249
	v_min_f32_e32 v249, v241, v249
	v_max_f32_e32 v241, v239, v247
	v_min_f32_e32 v247, v239, v247
	v_max_f32_e32 v239, v240, v248
	v_min_f32_e32 v248, v240, v248
	v_max_f32_e32 v240, v245, v253
	v_min_f32_e32 v253, v245, v253
	v_max_f32_e32 v245, v240, v248
	v_min_f32_e32 v248, v240, v248
	v_max_f32_e32 v240, v239, v241
	v_min_f32_e32 v241, v239, v241
	v_max_f32_e32 v239, v245, v247
	v_min_f32_e32 v247, v245, v247
	v_max_f32_e32 v245, v248, v249
	v_min_f32_e32 v249, v248, v249
	v_max_f32_e32 v248, v246, v238
	v_min_f32_e32 v238, v246, v238
	v_max_f32_e32 v246, v240, v244
	v_min_f32_e32 v244, v240, v244
	v_max_f32_e32 v240, v241, v128
	v_min_f32_e32 v128, v241, v128
	v_max_f32_e32 v241, v239, v243
	v_min_f32_e32 v243, v239, v243
	v_max_f32_e32 v239, v247, v242
	v_min_f32_e32 v242, v247, v242
	v_max_f32_e32 v247, v245, v252
	v_min_f32_e32 v252, v245, v252
	v_max_f32_e32 v245, v249, v250
	v_min_f32_e32 v250, v249, v250
	v_max_f32_e32 v236, v236, v253
	v_max_f32_e32 v254, v254, v250
	v_max_f32_e32 v226, v226, v245
	v_max_f32_e32 v225, v225, v252
	v_max_f32_e32 v229, v229, v247
	v_max_f32_e32 v232, v232, v242
	v_max_f32_e32 v234, v234, v239
	v_max_f32_e32 v233, v233, v243
	v_max_f32_e32 v230, v230, v241
	v_max_f32_e32 v231, v231, v128
	v_max_f32_e32 v235, v235, v240
	v_max_f32_e32 v228, v228, v244
	v_max_f32_e32 v222, v222, v246
; __device__ __forceinline__ float uniq_key(float s, int n) { return __uint_as_float((__float_as_uint(s) & ~0xffu) | (unsigned)(255 - n)); }
; #define INS16(A_, X_) do { float x_ = (X_); _Pragma("unroll") for (int i_ = 0; i_ < 16; ++i_) { const float hi_ = fmaxf(A_[i_], x_); x_ = fminf(A_[i_], x_); A_[i_] = hi_; } } while (0)
; __device__ __forceinline__ void p11_route(Frame& F) {
;     ...
;             for (int n = 0; n < PNK / 2; ++n) INS16(a, uniq_key(row[nb + n], nb + n));
;             float o[16];
; #pragma unroll
;             for (int i = 0; i < 16; ++i) o[i] = __builtin_bit_cast(float, __builtin_amdgcn_ds_bpermute(((F.lane + 32) & 63) << 2, __builtin_bit_cast(int, a[i])));
; #pragma unroll
;             for (int i = 0; i < 16; ++i) INS16(a, o[i]);
;           if (F.lane < 32) {
	v_max_f32_e32 v223, v223, v238
	v_max_f32_e32 v224, v224, v248
	v_max_f32_e32 v237, v237, v251
	v_max_f32_e32 v227, v236, v230
	v_min_f32_e32 v230, v236, v230
	v_max_f32_e32 v236, v254, v231
	v_min_f32_e32 v231, v254, v231
	v_max_f32_e32 v254, v226, v235
	v_min_f32_e32 v235, v226, v235
	v_max_f32_e32 v226, v225, v228
	v_min_f32_e32 v228, v225, v228
	v_max_f32_e32 v225, v229, v222
	v_min_f32_e32 v222, v229, v222
	v_max_f32_e32 v229, v232, v223
	v_min_f32_e32 v223, v232, v223
	v_max_f32_e32 v232, v234, v224
	v_min_f32_e32 v224, v234, v224
	v_max_f32_e32 v234, v233, v237
	v_min_f32_e32 v237, v233, v237
	v_max_f32_e32 v233, v227, v225
	v_min_f32_e32 v225, v227, v225
	v_max_f32_e32 v227, v236, v229
	v_min_f32_e32 v229, v236, v229
	v_max_f32_e32 v236, v254, v232
	v_min_f32_e32 v232, v254, v232
	v_max_f32_e32 v254, v226, v234
	v_min_f32_e32 v234, v226, v234
	v_max_f32_e32 v226, v230, v222
	v_min_f32_e32 v222, v230, v222
	v_max_f32_e32 v230, v231, v223
	v_min_f32_e32 v223, v231, v223
	v_max_f32_e32 v231, v235, v224
	v_min_f32_e32 v224, v235, v224
	v_max_f32_e32 v235, v228, v237
	v_min_f32_e32 v237, v228, v237
	v_max_f32_e32 v228, v233, v236
	v_min_f32_e32 v236, v233, v236
	v_max_f32_e32 v233, v227, v254
	v_min_f32_e32 v254, v227, v254
	v_max_f32_e32 v227, v225, v232
	v_min_f32_e32 v232, v225, v232
	v_max_f32_e32 v225, v229, v234
	v_min_f32_e32 v234, v229, v234
	v_max_f32_e32 v229, v226, v231
	v_min_f32_e32 v231, v226, v231
	v_max_f32_e32 v226, v230, v235
	v_min_f32_e32 v235, v230, v235
	v_max_f32_e32 v230, v222, v224
	v_min_f32_e32 v224, v222, v224
	v_max_f32_e32 v222, v223, v237
	v_min_f32_e32 v237, v223, v237
	v_max_f32_e32 v223, v228, v233
	v_min_f32_e32 v233, v228, v233
	v_max_f32_e32 v228, v236, v254
	v_min_f32_e32 v254, v236, v254
	v_max_f32_e32 v236, v227, v225
	v_min_f32_e32 v225, v227, v225
	v_max_f32_e32 v227, v232, v234
	v_min_f32_e32 v234, v232, v234
	v_max_f32_e32 v232, v229, v226
	v_min_f32_e32 v226, v229, v226
	v_max_f32_e32 v229, v231, v235
	v_min_f32_e32 v235, v231, v235
	v_max_f32_e32 v231, v230, v222
	v_min_f32_e32 v222, v230, v222
	v_max_f32_e32 v230, v224, v237
	v_min_f32_e32 v237, v224, v237
	v_mov_b32_e32 v137, v223
	v_mov_b32_e32 v139, v233
	v_mov_b32_e32 v140, v228
	v_mov_b32_e32 v141, v254
	v_mov_b32_e32 v142, v236
	v_mov_b32_e32 v143, v225
	v_mov_b32_e32 v144, v227
	v_mov_b32_e32 v145, v234
	v_mov_b32_e32 v147, v232
	v_mov_b32_e32 v148, v226
	v_mov_b32_e32 v149, v229
	v_mov_b32_e32 v159, v235
	v_mov_b32_e32 v161, v231
	v_mov_b32_e32 v162, v222
	v_mov_b32_e32 v160, v230
	v_mov_b32_e32 v129, v237
	ds_bpermute_b32 v166, v153, v137
	ds_bpermute_b32 v165, v153, v139
	ds_bpermute_b32 v164, v153, v140
	ds_bpermute_b32 v163, v153, v141
	ds_bpermute_b32 v146, v153, v142
	ds_bpermute_b32 v138, v153, v143
	ds_bpermute_b32 v136, v153, v144
	ds_bpermute_b32 v135, v153, v145
	ds_bpermute_b32 v134, v153, v147
	ds_bpermute_b32 v133, v153, v148
	ds_bpermute_b32 v132, v153, v149
	ds_bpermute_b32 v131, v153, v159
	ds_bpermute_b32 v130, v153, v161
	ds_bpermute_b32 v128, v153, v162
	ds_bpermute_b32 v127, v153, v160
	ds_bpermute_b32 v126, v153, v129
	s_and_saveexec_b64 s[4:5], s[0:1]
	s_cbranch_execz .LBB0_3218
; #define INS16(A_, X_) do { float x_ = (X_); _Pragma("unroll") for (int i_ = 0; i_ < 16; ++i_) { const float hi_ = fmaxf(A_[i_], x_); x_ = fminf(A_[i_], x_); A_[i_] = hi_; } } while (0)
; __device__ __forceinline__ void p11_route(Frame& F) {
;     ...
;             for (int i = 0; i < 16; ++i) INS16(a, o[i]);
;           if (F.lane < 32) {
;             float tv[16]; int ti[16];
; #pragma unroll
;             for (int i = 0; i < 16; ++i) { ti[i] = 255 - (int)(__float_as_uint(a[i]) & 255u); tv[i] = row[ti[i]]; }
; #pragma unroll
;             for (int i = 0; i < 16; ++i) { row[i] = tv[i]; row[16 + i] = __int_as_float(ti[i]); }
;           } }
	s_waitcnt lgkmcnt(0)
	v_max_f32_e32 v222, v137, v126
	v_max_f32_e32 v223, v139, v127
	v_max_f32_e32 v224, v140, v128
	v_max_f32_e32 v225, v141, v130
	v_max_f32_e32 v226, v142, v131
	v_max_f32_e32 v227, v143, v132
	v_max_f32_e32 v228, v144, v133
	v_max_f32_e32 v229, v145, v134
	v_max_f32_e32 v230, v147, v135
	v_max_f32_e32 v231, v148, v136
	v_max_f32_e32 v232, v149, v138
	v_max_f32_e32 v233, v159, v146
	v_max_f32_e32 v234, v161, v163
	v_max_f32_e32 v235, v162, v164
	v_max_f32_e32 v236, v160, v165
	v_max_f32_e32 v237, v129, v166
	v_max_f32_e32 v254, v222, v230
	v_min_f32_e32 v230, v222, v230
	v_max_f32_e32 v222, v223, v231
	v_min_f32_e32 v231, v223, v231
	v_max_f32_e32 v223, v224, v232
	v_min_f32_e32 v232, v224, v232
	v_max_f32_e32 v224, v225, v233
	v_min_f32_e32 v233, v225, v233
	v_max_f32_e32 v225, v226, v234
	v_min_f32_e32 v234, v226, v234
	v_max_f32_e32 v226, v227, v235
	v_min_f32_e32 v235, v227, v235
	v_max_f32_e32 v227, v228, v236
	v_min_f32_e32 v236, v228, v236
	v_max_f32_e32 v228, v229, v237
	v_min_f32_e32 v237, v229, v237
	v_max_f32_e32 v229, v254, v225
	v_min_f32_e32 v225, v254, v225
	v_max_f32_e32 v254, v222, v226
	v_min_f32_e32 v226, v222, v226
	v_max_f32_e32 v222, v223, v227
	v_min_f32_e32 v227, v223, v227
	v_max_f32_e32 v223, v224, v228
	v_min_f32_e32 v228, v224, v228
	v_max_f32_e32 v224, v230, v234
	v_min_f32_e32 v234, v230, v234
	v_max_f32_e32 v230, v231, v235
	v_min_f32_e32 v235, v231, v235
	v_max_f32_e32 v231, v232, v236
	v_min_f32_e32 v236, v232, v236
	v_max_f32_e32 v232, v233, v237
	v_min_f32_e32 v237, v233, v237
	v_max_f32_e32 v233, v229, v222
	v_min_f32_e32 v222, v229, v222
	v_max_f32_e32 v229, v254, v223
	v_min_f32_e32 v223, v254, v223
	v_max_f32_e32 v254, v225, v227
	v_min_f32_e32 v227, v225, v227
	v_max_f32_e32 v225, v226, v228
	v_min_f32_e32 v228, v226, v228
	v_max_f32_e32 v226, v224, v231
	v_min_f32_e32 v231, v224, v231
	v_max_f32_e32 v224, v230, v232
	v_min_f32_e32 v232, v230, v232
	v_max_f32_e32 v230, v234, v236
	v_min_f32_e32 v236, v234, v236
	v_max_f32_e32 v234, v235, v237
	v_min_f32_e32 v237, v235, v237
	v_max_f32_e32 v235, v233, v229
	v_min_f32_e32 v229, v233, v229
	v_max_f32_e32 v233, v222, v223
	v_min_f32_e32 v223, v222, v223
	v_max_f32_e32 v222, v254, v225
	v_min_f32_e32 v225, v254, v225
	v_max_f32_e32 v254, v227, v228
	v_min_f32_e32 v228, v227, v228
	v_max_f32_e32 v227, v226, v224
	v_min_f32_e32 v224, v226, v224
	v_max_f32_e32 v226, v231, v232
	v_min_f32_e32 v232, v231, v232
	v_max_f32_e32 v231, v230, v234
	v_min_f32_e32 v234, v230, v234
	v_max_f32_e32 v230, v236, v237
	v_min_f32_e32 v237, v236, v237
	v_mov_b32_e32 v126, v235
	v_mov_b32_e32 v127, v229
	v_mov_b32_e32 v128, v233
	v_mov_b32_e32 v130, v223
	v_mov_b32_e32 v131, v222
	v_mov_b32_e32 v132, v225
	v_mov_b32_e32 v133, v254
	v_mov_b32_e32 v134, v228
	v_mov_b32_e32 v135, v227
	v_mov_b32_e32 v136, v224
	v_mov_b32_e32 v137, v226
	v_mov_b32_e32 v138, v232
	v_mov_b32_e32 v139, v231
	v_mov_b32_e32 v140, v234
	v_mov_b32_e32 v141, v230
	v_mov_b32_e32 v129, v237
	v_xor_b32_e32 v127, -1, v127
	v_xor_b32_e32 v126, -1, v126
	v_xor_b32_e32 v130, -1, v130
	v_xor_b32_e32 v128, -1, v128
	v_xor_b32_e32 v132, -1, v132
	v_xor_b32_e32 v131, -1, v131
	v_xor_b32_e32 v134, -1, v134
	v_xor_b32_e32 v133, -1, v133
	v_xor_b32_e32 v136, -1, v136
	v_xor_b32_e32 v135, -1, v135
	v_xor_b32_e32 v138, -1, v138
	v_xor_b32_e32 v137, -1, v137
	v_xor_b32_e32 v140, -1, v140
	v_xor_b32_e32 v139, -1, v139
	v_xor_b32_e32 v129, -1, v129
	v_xor_b32_e32 v141, -1, v141
	v_and_b32_e32 v127, 0xff, v127
	v_and_b32_e32 v126, 0xff, v126
	v_and_b32_e32 v130, 0xff, v130
	v_and_b32_e32 v128, 0xff, v128
	v_and_b32_e32 v132, 0xff, v132
	v_and_b32_e32 v131, 0xff, v131
	v_and_b32_e32 v134, 0xff, v134
	v_and_b32_e32 v133, 0xff, v133
	v_and_b32_e32 v136, 0xff, v136
	v_and_b32_e32 v135, 0xff, v135
	v_and_b32_e32 v138, 0xff, v138
	v_and_b32_e32 v137, 0xff, v137
	v_and_b32_e32 v140, 0xff, v140
	v_and_b32_e32 v139, 0xff, v139
	v_and_b32_e32 v129, 0xff, v129
	v_and_b32_e32 v141, 0xff, v141
	v_lshl_add_u32 v142, v126, 2, v152
	v_lshl_add_u32 v143, v127, 2, v152
	v_lshl_add_u32 v144, v128, 2, v152
	v_lshl_add_u32 v145, v130, 2, v152
	v_lshl_add_u32 v146, v131, 2, v152
	v_lshl_add_u32 v147, v132, 2, v152
	v_lshl_add_u32 v148, v133, 2, v152
	v_lshl_add_u32 v149, v134, 2, v152
	v_lshl_add_u32 v159, v135, 2, v152
	v_lshl_add_u32 v160, v136, 2, v152
	v_lshl_add_u32 v161, v137, 2, v152
	v_lshl_add_u32 v162, v138, 2, v152
	v_lshl_add_u32 v163, v139, 2, v152
	v_lshl_add_u32 v164, v140, 2, v152
	v_lshl_add_u32 v165, v141, 2, v152
	v_lshl_add_u32 v166, v129, 2, v152
	ds_read_b32 v142, v142
	ds_read_b32 v143, v143
	ds_read_b32 v144, v144
	ds_read_b32 v145, v145
	ds_read_b32 v146, v146
	ds_read_b32 v147, v147
	ds_read_b32 v148, v148
	ds_read_b32 v149, v149
	ds_read_b32 v159, v159
	ds_read_b32 v160, v160
	ds_read_b32 v161, v161
	ds_read_b32 v162, v162
	ds_read_b32 v163, v163
	ds_read_b32 v164, v164
	ds_read_b32 v165, v165
	ds_read_b32 v166, v166
	s_waitcnt lgkmcnt(14)
	ds_write2_b32 v152, v142, v143 offset1:1
	ds_write2_b32 v152, v126, v127 offset0:16 offset1:17
	s_waitcnt lgkmcnt(14)
	ds_write2_b32 v152, v144, v145 offset0:2 offset1:3
	ds_write2_b32 v152, v128, v130 offset0:18 offset1:19
	s_waitcnt lgkmcnt(14)
	ds_write2_b32 v152, v146, v147 offset0:4 offset1:5
	ds_write2_b32 v152, v131, v132 offset0:20 offset1:21
	s_waitcnt lgkmcnt(14)
	ds_write2_b32 v152, v148, v149 offset0:6 offset1:7
	ds_write2_b32 v152, v133, v134 offset0:22 offset1:23
	s_waitcnt lgkmcnt(14)
	ds_write2_b32 v152, v159, v160 offset0:8 offset1:9
	ds_write2_b32 v152, v135, v136 offset0:24 offset1:25
	s_waitcnt lgkmcnt(14)
	ds_write2_b32 v152, v161, v162 offset0:10 offset1:11
	ds_write2_b32 v152, v137, v138 offset0:26 offset1:27
	s_waitcnt lgkmcnt(14)
	ds_write2_b32 v152, v163, v164 offset0:12 offset1:13
	ds_write2_b32 v152, v139, v140 offset0:28 offset1:29
	s_waitcnt lgkmcnt(14)
	ds_write2_b32 v152, v165, v166 offset0:14 offset1:15
	ds_write2_b32 v152, v141, v129 offset0:30 offset1:31
	s_or_b64 exec, exec, s[4:5]
	s_and_saveexec_b64 s[12:13], s[2:3]
	s_cbranch_execz .LBB0_3213
	s_branch .LBB0_3219
